# conv+SiLU phase and pool/head-norm phase: nt (streaming) hint on their read-once row loads
# speedup vs baseline: 1.0151x; 1.0101x over previous
; __device__ __forceinline__ void p3_conv(const Args& a, const Frame& F) {
;     ...
;     const int cg = F.tid & 127, sub = F.tid >> 7, c0 = cg * 8;
;     float w0[8], w1[8], w2[8], bb[8];
; #pragma unroll
;     for (int j = 0; j < 8; ++j) { w0[j] = cw[c0 + j]; w1[j] = cw[1024 + c0 + j]; w2[j] = cw[2048 + c0 + j]; bb[j] = cb[c0 + j]; }
;     const float scl = c0 < 512 ? 0.08838834764831845f : 1.0f;
;     const u32x4 z = (u32x4){0u, 0u, 0u, 0u};
;     for (int item = F.bid * 4 + sub; item < TA / 16; item += F.G * 4) {
.LBB0_340:
	s_cmp_lt_i32 s74, 4
	s_cselect_b64 s[4:5], -1, 0
	s_and_b64 s[0:1], s[4:5], s[0:1]
	s_andn2_b64 vcc, exec, s[0:1]
	v_lshrrev_b32_e32 v208, 7, v0
	s_cbranch_vccnz .LBB0_381
	v_lshrrev_b32_e32 v34, 7, v0
	v_lshl_or_b32 v1, s2, 2, v34
	s_movk_i32 s4, 0x1080
	v_cmp_gt_i32_e32 vcc, s4, v1
	s_and_saveexec_b64 s[4:5], vcc
	s_cbranch_execz .LBB0_380
	v_lshlrev_b32_e32 v2, 3, v0
	v_and_b32_e32 v35, 0x3f8, v2
	v_lshlrev_b32_e32 v36, 2, v35
	v_mov_b32_e32 v37, 0
	v_lshl_add_u64 v[30:31], s[54:55], 0, v[36:37]
	s_movk_i32 s10, 0x1000
	v_add_co_u32_e32 v22, vcc, s10, v30
	s_movk_i32 s8, 0x2000
	s_nop 0
	v_addc_co_u32_e32 v23, vcc, 0, v31, vcc
	global_load_dwordx4 v[2:5], v36, s[56:57] offset:16
	global_load_dwordx4 v[6:9], v36, s[56:57]
	s_mov_b64 s[6:7], 0x2000
	global_load_dwordx4 v[10:13], v36, s[54:55]
	global_load_dwordx4 v[14:17], v36, s[54:55] offset:16
	global_load_dwordx4 v[18:21], v[22:23], off nt
	v_add_co_u32_e32 v22, vcc, s8, v30
	s_mov_b64 s[8:9], 0x1000
	s_nop 0
	v_addc_co_u32_e32 v23, vcc, 0, v31, vcc
	v_lshl_add_u64 v[26:27], v[30:31], 0, s[8:9]
	v_lshl_add_u64 v[30:31], v[30:31], 0, s[6:7]
	global_load_dwordx4 v[22:25], v[22:23], off nt
	s_movk_i32 s20, 0x200
	global_load_dwordx4 v[26:29], v[26:27], off offset:16 nt
	v_mov_b32_e32 v36, 0x3db504f3
	global_load_dwordx4 v[30:33], v[30:31], off offset:16 nt
	v_lshlrev_b32_e32 v34, 4, v34
	v_cmp_gt_u32_e32 vcc, s20, v35
	v_lshl_or_b32 v34, s2, 6, v34
	s_mov_b64 s[8:9], 0xac00000
	v_cndmask_b32_e32 v104, 1.0, v36, vcc
	v_lshlrev_b32_e32 v36, 1, v35
	s_mov_b64 s[16:17], 0x2800000
	v_add_u32_e32 v106, -1, v34
	v_lshl_add_u64 v[34:35], s[72:73], 0, v[36:37]
	s_lshl_b32 s11, s3, 2
	s_lshl_b32 s12, s3, 6
	s_mov_b64 s[6:7], 0
	s_mov_b32 s13, 0xffff0000
	s_movk_i32 s14, 0x7fff
	s_movk_i32 s15, 0x107f
	v_mov_b32_e32 v146, 0x100
	v_mov_b32_e32 v147, 0x2000
	v_mov_b32_e32 v148, 0xf0
	v_mov_b32_e32 v105, v104
	v_lshl_add_u64 v[108:109], v[34:35], 0, s[8:9]
	v_lshl_add_u64 v[110:111], v[34:35], 0, s[16:17]
	v_mov_b32_e32 v149, 0x1ff0
	s_waitcnt vmcnt(0)
	v_mov_b32_e32 v112, v7
	v_mov_b32_e32 v113, v9
	v_mov_b32_e32 v114, v11
	v_mov_b32_e32 v115, v13
	v_mov_b32_e32 v7, v8
	v_mov_b32_e32 v11, v12
	v_mov_b32_e32 v8, v3
	v_mov_b32_e32 v9, v5
	v_mov_b32_e32 v12, v15
	v_mov_b32_e32 v13, v17
	v_mov_b32_e32 v3, v4
	v_mov_b32_e32 v15, v16
	v_mov_b32_e32 v4, v19
	v_mov_b32_e32 v5, v21
	v_mov_b32_e32 v16, v23
	v_mov_b32_e32 v17, v25
	v_mov_b32_e32 v19, v20
	v_mov_b32_e32 v23, v24
	v_mov_b32_e32 v20, v27
	v_mov_b32_e32 v21, v29
	v_mov_b32_e32 v24, v31
	v_mov_b32_e32 v25, v33
	v_mov_b32_e32 v27, v28
	v_mov_b32_e32 v31, v32
	s_branch .LBB0_344

; __device__ __forceinline__ void p3_conv(const Args& a, const Frame& F) {
;     ...
;         const int r0 = item * 16;
;         const int len = (r0 < T) ? SEQ : CTXL, pos0 = (r0 < T) ? (r0 & (SEQ - 1)) : ((r0 - T) & (CTXL - 1));
;         u32x4 rw[18];
; #pragma unroll
;         for (int i = 0; i < 18; ++i) { const int pos = pos0 + i - 1; rw[i] = (pos >= 0 && pos < len) ? *(const u32x4*)(PQK + (size_t)(r0 + i - 1) * 1024 + c0) : z; }
.LBB0_344:
	v_cmp_gt_i32_e32 vcc, s10, v1
	v_add_u32_e32 v144, 1, v106
	v_mov_b32_e32 v96, 0
	v_cndmask_b32_e32 v28, v148, v149, vcc
	v_and_b32_e32 v33, v28, v144
	v_cndmask_b32_e32 v32, v146, v147, vcc
	v_add_u32_e32 v28, -1, v33
	v_cmp_lt_u32_e32 vcc, v28, v32
	v_mov_b32_e32 v97, 0
	v_mov_b32_e32 v98, 0
	v_mov_b32_e32 v99, 0
	s_and_saveexec_b64 s[8:9], vcc
	s_cbranch_execz .LBB0_346
	v_ashrrev_i32_e32 v107, 31, v106
	v_lshlrev_b64 v[28:29], 11, v[106:107]
	v_lshl_add_u64 v[28:29], v[108:109], 0, v[28:29]
	global_load_dwordx4 v[96:99], v[28:29], off nt
.LBB0_346:
	s_or_b64 exec, exec, s[8:9]
	v_cmp_lt_u32_e32 vcc, v33, v32
	v_mov_b32_e32 v92, 0
	v_ashrrev_i32_e32 v145, 31, v144
	v_mov_b32_e32 v100, 0
	v_mov_b32_e32 v101, 0
	v_mov_b32_e32 v102, 0
	v_mov_b32_e32 v103, 0
	s_and_saveexec_b64 s[8:9], vcc
	s_cbranch_execz .LBB0_348
	v_lshlrev_b64 v[28:29], 11, v[144:145]
	v_lshl_add_u64 v[28:29], v[108:109], 0, v[28:29]
	global_load_dwordx4 v[100:103], v[28:29], off nt
.LBB0_348:
	s_or_b64 exec, exec, s[8:9]
	v_or_b32_e32 v28, 1, v33
	v_add_u32_e32 v142, 2, v106
	v_cmp_lt_u32_e32 vcc, v28, v32
	v_ashrrev_i32_e32 v143, 31, v142
	v_mov_b32_e32 v93, 0
	v_mov_b32_e32 v94, 0
	v_mov_b32_e32 v95, 0
	s_and_saveexec_b64 s[8:9], vcc
	s_cbranch_execz .LBB0_350
	v_lshlrev_b64 v[28:29], 11, v[142:143]
	v_lshl_add_u64 v[28:29], v[108:109], 0, v[28:29]
	global_load_dwordx4 v[92:95], v[28:29], off nt
.LBB0_350:
	s_or_b64 exec, exec, s[8:9]
	v_or_b32_e32 v28, 2, v33
	v_add_u32_e32 v140, 3, v106
	v_cmp_lt_u32_e32 vcc, v28, v32
	v_mov_b32_e32 v84, 0
	v_ashrrev_i32_e32 v141, 31, v140
	v_mov_b32_e32 v88, 0
	v_mov_b32_e32 v89, 0
	v_mov_b32_e32 v90, 0
	v_mov_b32_e32 v91, 0
	s_and_saveexec_b64 s[8:9], vcc
	s_cbranch_execz .LBB0_352
	v_lshlrev_b64 v[28:29], 11, v[140:141]
	v_lshl_add_u64 v[28:29], v[108:109], 0, v[28:29]
	global_load_dwordx4 v[88:91], v[28:29], off nt
.LBB0_352:
	s_or_b64 exec, exec, s[8:9]
	v_or_b32_e32 v28, 3, v33
	v_add_u32_e32 v138, 4, v106
	v_cmp_lt_u32_e32 vcc, v28, v32
	v_ashrrev_i32_e32 v139, 31, v138
	v_mov_b32_e32 v85, 0
	v_mov_b32_e32 v86, 0
	v_mov_b32_e32 v87, 0
	s_and_saveexec_b64 s[8:9], vcc
	s_cbranch_execz .LBB0_354
	v_lshlrev_b64 v[28:29], 11, v[138:139]
	v_lshl_add_u64 v[28:29], v[108:109], 0, v[28:29]
	global_load_dwordx4 v[84:87], v[28:29], off nt
.LBB0_354:
	s_or_b64 exec, exec, s[8:9]
	v_or_b32_e32 v28, 4, v33
	v_add_u32_e32 v136, 5, v106
	v_cmp_lt_u32_e32 vcc, v28, v32
	v_mov_b32_e32 v76, 0
	v_ashrrev_i32_e32 v137, 31, v136
	v_mov_b32_e32 v80, 0
	v_mov_b32_e32 v81, 0
	v_mov_b32_e32 v82, 0
	v_mov_b32_e32 v83, 0
	s_and_saveexec_b64 s[8:9], vcc
	s_cbranch_execz .LBB0_356
	v_lshlrev_b64 v[28:29], 11, v[136:137]
	v_lshl_add_u64 v[28:29], v[108:109], 0, v[28:29]
	global_load_dwordx4 v[80:83], v[28:29], off nt
.LBB0_356:
	s_or_b64 exec, exec, s[8:9]
	v_or_b32_e32 v28, 5, v33
	v_add_u32_e32 v134, 6, v106
	v_cmp_lt_u32_e32 vcc, v28, v32
	v_ashrrev_i32_e32 v135, 31, v134
	v_mov_b32_e32 v77, 0
	v_mov_b32_e32 v78, 0
	v_mov_b32_e32 v79, 0
	s_and_saveexec_b64 s[8:9], vcc
	s_cbranch_execz .LBB0_358
	v_lshlrev_b64 v[28:29], 11, v[134:135]
	v_lshl_add_u64 v[28:29], v[108:109], 0, v[28:29]
	global_load_dwordx4 v[76:79], v[28:29], off nt
.LBB0_358:
	s_or_b64 exec, exec, s[8:9]
	v_or_b32_e32 v28, 6, v33
	v_add_u32_e32 v132, 7, v106
	v_cmp_lt_u32_e32 vcc, v28, v32
	v_mov_b32_e32 v68, 0
	v_ashrrev_i32_e32 v133, 31, v132
	v_mov_b32_e32 v72, 0
	v_mov_b32_e32 v73, 0
	v_mov_b32_e32 v74, 0
	v_mov_b32_e32 v75, 0
	s_and_saveexec_b64 s[8:9], vcc
	s_cbranch_execz .LBB0_360
	v_lshlrev_b64 v[28:29], 11, v[132:133]
	v_lshl_add_u64 v[28:29], v[108:109], 0, v[28:29]
	global_load_dwordx4 v[72:75], v[28:29], off nt
.LBB0_360:
	s_or_b64 exec, exec, s[8:9]
	v_or_b32_e32 v28, 7, v33
	v_add_u32_e32 v130, 8, v106
	v_cmp_lt_u32_e32 vcc, v28, v32
	v_ashrrev_i32_e32 v131, 31, v130
	v_mov_b32_e32 v69, 0
	v_mov_b32_e32 v70, 0
	v_mov_b32_e32 v71, 0
	s_and_saveexec_b64 s[8:9], vcc
	s_cbranch_execz .LBB0_362
	v_lshlrev_b64 v[28:29], 11, v[130:131]
	v_lshl_add_u64 v[28:29], v[108:109], 0, v[28:29]
	global_load_dwordx4 v[68:71], v[28:29], off nt
; __device__ __forceinline__ void p3_conv(const Args& a, const Frame& F) {
;     ...
;         const int r0 = item * 16;
;         const int len = (r0 < T) ? SEQ : CTXL, pos0 = (r0 < T) ? (r0 & (SEQ - 1)) : ((r0 - T) & (CTXL - 1));
;         u32x4 rw[18];
; #pragma unroll
;         for (int i = 0; i < 18; ++i) { const int pos = pos0 + i - 1; rw[i] = (pos >= 0 && pos < len) ? *(const u32x4*)(PQK + (size_t)(r0 + i - 1) * 1024 + c0) : z; }
.LBB0_362:
	s_or_b64 exec, exec, s[8:9]
	v_or_b32_e32 v28, 8, v33
	v_add_u32_e32 v128, 9, v106
	v_cmp_lt_u32_e32 vcc, v28, v32
	v_mov_b32_e32 v60, 0
	v_ashrrev_i32_e32 v129, 31, v128
	v_mov_b32_e32 v64, 0
	v_mov_b32_e32 v65, 0
	v_mov_b32_e32 v66, 0
	v_mov_b32_e32 v67, 0
	s_and_saveexec_b64 s[8:9], vcc
	s_cbranch_execz .LBB0_364
	v_lshlrev_b64 v[28:29], 11, v[128:129]
	v_lshl_add_u64 v[28:29], v[108:109], 0, v[28:29]
	global_load_dwordx4 v[64:67], v[28:29], off nt
.LBB0_364:
	s_or_b64 exec, exec, s[8:9]
	v_or_b32_e32 v28, 9, v33
	v_add_u32_e32 v126, 10, v106
	v_cmp_lt_u32_e32 vcc, v28, v32
	v_ashrrev_i32_e32 v127, 31, v126
	v_mov_b32_e32 v61, 0
	v_mov_b32_e32 v62, 0
	v_mov_b32_e32 v63, 0
	s_and_saveexec_b64 s[8:9], vcc
	s_cbranch_execz .LBB0_366
	v_lshlrev_b64 v[28:29], 11, v[126:127]
	v_lshl_add_u64 v[28:29], v[108:109], 0, v[28:29]
	global_load_dwordx4 v[60:63], v[28:29], off nt
.LBB0_366:
	s_or_b64 exec, exec, s[8:9]
	v_or_b32_e32 v28, 10, v33
	v_add_u32_e32 v124, 11, v106
	v_cmp_lt_u32_e32 vcc, v28, v32
	v_mov_b32_e32 v52, 0
	v_ashrrev_i32_e32 v125, 31, v124
	v_mov_b32_e32 v56, 0
	v_mov_b32_e32 v57, 0
	v_mov_b32_e32 v58, 0
	v_mov_b32_e32 v59, 0
	s_and_saveexec_b64 s[8:9], vcc
	s_cbranch_execz .LBB0_368
	v_lshlrev_b64 v[28:29], 11, v[124:125]
	v_lshl_add_u64 v[28:29], v[108:109], 0, v[28:29]
	global_load_dwordx4 v[56:59], v[28:29], off nt
.LBB0_368:
	s_or_b64 exec, exec, s[8:9]
	v_or_b32_e32 v28, 11, v33
	v_add_u32_e32 v122, 12, v106
	v_cmp_lt_u32_e32 vcc, v28, v32
	v_ashrrev_i32_e32 v123, 31, v122
	v_mov_b32_e32 v53, 0
	v_mov_b32_e32 v54, 0
	v_mov_b32_e32 v55, 0
	s_and_saveexec_b64 s[8:9], vcc
	s_cbranch_execz .LBB0_370
	v_lshlrev_b64 v[28:29], 11, v[122:123]
	v_lshl_add_u64 v[28:29], v[108:109], 0, v[28:29]
	global_load_dwordx4 v[52:55], v[28:29], off nt
.LBB0_370:
	s_or_b64 exec, exec, s[8:9]
	v_or_b32_e32 v28, 12, v33
	v_add_u32_e32 v120, 13, v106
	v_cmp_lt_u32_e32 vcc, v28, v32
	v_mov_b32_e32 v44, 0
	v_ashrrev_i32_e32 v121, 31, v120
	v_mov_b32_e32 v48, 0
	v_mov_b32_e32 v49, 0
	v_mov_b32_e32 v50, 0
	v_mov_b32_e32 v51, 0
	s_and_saveexec_b64 s[8:9], vcc
	s_cbranch_execz .LBB0_372
	v_lshlrev_b64 v[28:29], 11, v[120:121]
	v_lshl_add_u64 v[28:29], v[108:109], 0, v[28:29]
	global_load_dwordx4 v[48:51], v[28:29], off nt
.LBB0_372:
	s_or_b64 exec, exec, s[8:9]
	v_or_b32_e32 v28, 13, v33
	v_add_u32_e32 v118, 14, v106
	v_cmp_lt_u32_e32 vcc, v28, v32
	v_ashrrev_i32_e32 v119, 31, v118
	v_mov_b32_e32 v45, 0
	v_mov_b32_e32 v46, 0
	v_mov_b32_e32 v47, 0
	s_and_saveexec_b64 s[8:9], vcc
	s_cbranch_execz .LBB0_374
	v_lshlrev_b64 v[28:29], 11, v[118:119]
	v_lshl_add_u64 v[28:29], v[108:109], 0, v[28:29]
	global_load_dwordx4 v[44:47], v[28:29], off nt
.LBB0_374:
	s_or_b64 exec, exec, s[8:9]
	v_or_b32_e32 v28, 14, v33
	v_add_u32_e32 v116, 15, v106
	v_cmp_lt_u32_e32 vcc, v28, v32
	v_mov_b32_e32 v36, 0
	v_ashrrev_i32_e32 v117, 31, v116
	v_mov_b32_e32 v40, 0
	v_mov_b32_e32 v41, 0
	v_mov_b32_e32 v42, 0
	v_mov_b32_e32 v43, 0
	s_and_saveexec_b64 s[8:9], vcc
	s_cbranch_execz .LBB0_376
	v_lshlrev_b64 v[28:29], 11, v[116:117]
	v_lshl_add_u64 v[28:29], v[108:109], 0, v[28:29]
	global_load_dwordx4 v[40:43], v[28:29], off nt
.LBB0_376:
	s_or_b64 exec, exec, s[8:9]
	v_or_b32_e32 v28, 15, v33
	v_cmp_lt_u32_e32 vcc, v28, v32
	v_add_u32_e32 v28, 16, v106
	v_ashrrev_i32_e32 v29, 31, v28
	v_mov_b32_e32 v37, 0
	v_mov_b32_e32 v38, 0
	v_mov_b32_e32 v39, 0
	s_and_saveexec_b64 s[8:9], vcc
	s_cbranch_execz .LBB0_378
	v_lshlrev_b64 v[34:35], 11, v[28:29]
	v_lshl_add_u64 v[34:35], v[108:109], 0, v[34:35]
	global_load_dwordx4 v[36:39], v[34:35], off nt
.LBB0_378:
	s_or_b64 exec, exec, s[8:9]
	v_add_u32_e32 v33, 16, v33
	v_cmp_lt_u32_e32 vcc, v33, v32
	v_mov_b32_e32 v32, 0
	v_mov_b32_e32 v33, 0
	v_mov_b32_e32 v34, 0
	v_mov_b32_e32 v35, 0
	s_and_saveexec_b64 s[8:9], vcc
	s_cbranch_execz .LBB0_343
	v_add_u32_e32 v32, 17, v106
	v_ashrrev_i32_e32 v33, 31, v32
	v_lshlrev_b64 v[32:33], 11, v[32:33]
	v_lshl_add_u64 v[32:33], v[108:109], 0, v[32:33]
	global_load_dwordx4 v[32:35], v[32:33], off nt
	s_branch .LBB0_343

; #define LAS __attribute__((address_space(3)))
; __device__ __forceinline__ void p5_pool_yb(const Args& a, const Frame& F) {
;     ...
;     for (int item = F.bid; item < T / 64; item += F.G) {
;         __syncthreads();
; #pragma unroll
;         for (int i = 0; i < 8; ++i) { const int p = F.tid + 512 * i, row = p >> 6, c16 = p & 63; *(LAS u32x4*)(L + row * 1024 + c16 * 16) = *(const u32x4*)(PP + (size_t)(item * 64 + row) * 512 + c16 * 8); }
;         __syncthreads();
.LBB0_567:
	s_lshl_b32 s0, s14, 6
	v_or_b32_e32 v6, s0, v1
	v_ashrrev_i32_e32 v7, 31, v6
	v_or_b32_e32 v8, s0, v16
	v_lshlrev_b64 v[6:7], 10, v[6:7]
	v_ashrrev_i32_e32 v9, 31, v8
	v_lshl_add_u64 v[6:7], v[2:3], 0, v[6:7]
	v_lshlrev_b64 v[8:9], 10, v[8:9]
	s_waitcnt vmcnt(0) lgkmcnt(0)
	s_barrier
	v_lshl_add_u64 v[8:9], v[2:3], 0, v[8:9]
	global_load_dwordx4 v[40:43], v[6:7], off nt
	global_load_dwordx4 v[44:47], v[8:9], off nt
	v_or_b32_e32 v6, s0, v17
	v_ashrrev_i32_e32 v7, 31, v6
	v_or_b32_e32 v8, s0, v18
	v_lshlrev_b64 v[6:7], 10, v[6:7]
	v_ashrrev_i32_e32 v9, 31, v8
	v_lshl_add_u64 v[6:7], v[2:3], 0, v[6:7]
	v_lshlrev_b64 v[8:9], 10, v[8:9]
	v_lshl_add_u64 v[8:9], v[2:3], 0, v[8:9]
	global_load_dwordx4 v[48:51], v[6:7], off nt
	global_load_dwordx4 v[52:55], v[8:9], off nt
	v_or_b32_e32 v6, s0, v19
	v_ashrrev_i32_e32 v7, 31, v6
	v_or_b32_e32 v8, s0, v20
	v_lshlrev_b64 v[6:7], 10, v[6:7]
	v_ashrrev_i32_e32 v9, 31, v8
	v_lshl_add_u64 v[6:7], v[2:3], 0, v[6:7]
	v_lshlrev_b64 v[8:9], 10, v[8:9]
	v_lshl_add_u64 v[8:9], v[2:3], 0, v[8:9]
	global_load_dwordx4 v[56:59], v[6:7], off nt
	global_load_dwordx4 v[60:63], v[8:9], off nt
	v_or_b32_e32 v6, s0, v21
	v_ashrrev_i32_e32 v7, 31, v6
	v_or_b32_e32 v8, s0, v22
	v_lshlrev_b64 v[6:7], 10, v[6:7]
	v_ashrrev_i32_e32 v9, 31, v8
	v_lshl_add_u64 v[6:7], v[2:3], 0, v[6:7]
	v_lshlrev_b64 v[8:9], 10, v[8:9]
	v_lshl_add_u64 v[8:9], v[2:3], 0, v[8:9]
	global_load_dwordx4 v[64:67], v[6:7], off nt
	global_load_dwordx4 v[68:71], v[8:9], off nt
	v_mov_b32_e32 v7, 0
	v_mov_b32_e32 v6, 0
	v_mov_b32_e32 v15, 0
	v_mov_b32_e32 v14, 0
	v_mov_b32_e32 v13, 0
	v_mov_b32_e32 v12, 0
	v_mov_b32_e32 v9, 0
	v_mov_b32_e32 v8, 0
	s_waitcnt vmcnt(7)
	ds_write_b128 v32, v[40:43]
	s_waitcnt vmcnt(6)
	ds_write_b128 v33, v[44:47]
	s_waitcnt vmcnt(5)
	ds_write_b128 v34, v[48:51]
	s_waitcnt vmcnt(4)
	ds_write_b128 v35, v[52:55]
	s_waitcnt vmcnt(3)
	ds_write_b128 v36, v[56:59]
	s_waitcnt vmcnt(2)
	ds_write_b128 v37, v[60:63]
	s_waitcnt vmcnt(1)
	ds_write_b128 v38, v[64:67]
	s_waitcnt vmcnt(0)
	ds_write_b128 v39, v[68:71]
	s_waitcnt lgkmcnt(0)
	s_barrier
	s_and_saveexec_b64 s[4:5], vcc
	s_cbranch_execz .LBB0_571
	v_mov_b32_e32 v6, 0
	s_mov_b64 s[6:7], 0
	v_mov_b32_e32 v40, v28
	v_mov_b32_e32 v41, v24
	v_mov_b32_e32 v7, v6
	v_mov_b32_e32 v8, v6
	v_mov_b32_e32 v9, v6
	v_mov_b32_e32 v12, v6
	v_mov_b32_e32 v13, v6
	v_mov_b32_e32 v14, v6
	v_mov_b32_e32 v15, v6

; __device__ __forceinline__ float bflo(unsigned w) { return __uint_as_float(w << 16); }
; __device__ __forceinline__ float bfhi(unsigned w) { return __uint_as_float(w & 0xffff0000u); }
; __device__ __forceinline__ float sigmoidf_(float x) { return frcp_(1.0f + fexp_(-x)); }
; __device__ __forceinline__ void p5_pool_yb(const Args& a, const Frame& F) {
;     ...
;     const bf16* HF = (const bf16*)(a.ws + WS_HF); const bf16* HB = (const bf16*)(a.ws + WS_HB); const bf16* POg = (const bf16*)(a.ws + WS_PO); bf16* YB = (bf16*)(a.ws + WS_YB);
;     const int gw = F.bid * 8 + F.wave, NGW = F.G * 8;
;     const f32x4 hw0 = *(const f32x4*)(a.in[IN_HNW] + F.lane * 8), hw1 = *(const f32x4*)(a.in[IN_HNW] + F.lane * 8 + 4);
;     const float hwv[8] = {hw0.x, hw0.y, hw0.z, hw0.w, hw1.x, hw1.y, hw1.z, hw1.w};
;     for (int t0 = gw * 4; t0 < T; t0 += NGW * 4) {
;         u32x4 f[4], bk[4], og[4];
; #pragma unroll
;         for (int u = 0; u < 4; ++u) { const size_t o = (size_t)(t0 + u) * 512 + F.lane * 8; f[u] = *(const u32x4*)(HF + o); bk[u] = *(const u32x4*)(HB + o); og[u] = *(const u32x4*)(POg + o); }
; #pragma unroll
;         for (int u = 0; u < 4; ++u) {
;             float v[8];
;             v[0] = bflo(f[u].x) + bflo(bk[u].x); v[1] = bfhi(f[u].x) + bfhi(bk[u].x); v[2] = bflo(f[u].y) + bflo(bk[u].y); v[3] = bfhi(f[u].y) + bfhi(bk[u].y);
;             v[4] = bflo(f[u].z) + bflo(bk[u].z); v[5] = bfhi(f[u].z) + bfhi(bk[u].z); v[6] = bflo(f[u].w) + bflo(bk[u].w); v[7] = bfhi(f[u].w) + bfhi(bk[u].w);
;             float s2 = 0.f;
; #pragma unroll
;             for (int jj = 0; jj < 8; ++jj) s2 += v[jj] * v[jj];
; #pragma unroll
;             for (int o = 1; o < 16; o <<= 1) s2 += __shfl_xor(s2, o);
;             const float rstd = rsqrtf(s2 * (1.f / 128.f) + EPS);
;             float gsig[8];
;             gsig[0] = sigmoidf_(bflo(og[u].x)); gsig[1] = sigmoidf_(bfhi(og[u].x)); gsig[2] = sigmoidf_(bflo(og[u].y)); gsig[3] = sigmoidf_(bfhi(og[u].y));
;             gsig[4] = sigmoidf_(bflo(og[u].z)); gsig[5] = sigmoidf_(bfhi(og[u].z)); gsig[6] = sigmoidf_(bflo(og[u].w)); gsig[7] = sigmoidf_(bfhi(og[u].w));
.LBB0_577:
	s_lshl_b32 s0, s2, 5
	s_lshl_b32 s1, s96, 2
	s_add_i32 s10, s1, s0
	s_cmp_gt_i32 s10, 0xffff
	s_cbranch_scc1 .LBB0_580
	v_mov_b32_e32 v2, s62
	v_mov_b32_e32 v3, s63
	v_lshl_add_u64 v[12:13], v[10:11], 2, v[2:3]
	global_load_dwordx4 v[2:5], v[12:13], off nt
	global_load_dwordx4 v[6:9], v[12:13], off offset:16 nt
	v_mbcnt_lo_u32_b32 v1, -1, 0
	v_mbcnt_hi_u32_b32 v12, -1, v1
	v_and_b32_e32 v1, 64, v12
	v_add_u32_e32 v13, 64, v1
	v_xor_b32_e32 v1, 1, v12
	v_cmp_lt_i32_e32 vcc, v1, v13
	v_xor_b32_e32 v14, 2, v12
	s_ashr_i32 s11, s10, 31
	v_cndmask_b32_e32 v1, v12, v1, vcc
	v_cmp_lt_i32_e32 vcc, v14, v13
	s_lshl_b32 s12, s3, 5
	s_lshl_b64 s[0:1], s[10:11], 10
	v_cndmask_b32_e32 v14, v12, v14, vcc
	v_lshlrev_b32_e32 v32, 2, v14
	v_xor_b32_e32 v14, 4, v12
	v_cmp_lt_i32_e32 vcc, v14, v13
	s_add_u32 s0, s72, s0
	s_addc_u32 s1, s73, s1
	v_cndmask_b32_e32 v14, v12, v14, vcc
	v_lshlrev_b32_e32 v33, 2, v14
	v_xor_b32_e32 v14, 8, v12
	v_cmp_lt_i32_e32 vcc, v14, v13
	v_lshl_add_u64 v[10:11], v[10:11], 1, s[0:1]
	s_mov_b64 s[0:1], 0x1b200c00
	v_cndmask_b32_e32 v12, v12, v14, vcc
	s_ashr_i32 s13, s12, 31
	v_lshlrev_b32_e32 v1, 2, v1
	v_lshlrev_b32_e32 v34, 2, v12
	v_lshl_add_u64 v[26:27], v[10:11], 0, s[0:1]
	s_lshl_b64 s[14:15], s[12:13], 10
	v_mov_b32_e32 v35, 0x358637bd
	s_mov_b32 s11, 0x800000
	s_mov_b32 s13, 0xeb600000
.LBB0_579:
	v_add_co_u32_e32 v30, vcc, 0xefa00000, v26
	global_load_dwordx4 v[22:25], v[26:27], off offset:-3072 nt
	global_load_dwordx4 v[18:21], v[26:27], off offset:-2048 nt
	global_load_dwordx4 v[14:17], v[26:27], off offset:-1024 nt
	global_load_dwordx4 v[10:13], v[26:27], off nt
	v_addc_co_u32_e32 v31, vcc, -1, v27, vcc
	v_add_co_u32_e32 v68, vcc, 0xf3a00000, v26
	global_load_dwordx4 v[36:39], v[30:31], off offset:-3072 nt
	s_nop 0
	v_addc_co_u32_e32 v69, vcc, -1, v27, vcc
	global_load_dwordx4 v[40:43], v[30:31], off offset:-2048 nt
	global_load_dwordx4 v[44:47], v[30:31], off offset:-1024 nt
	global_load_dwordx4 v[48:51], v[30:31], off nt
	global_load_dwordx4 v[52:55], v[68:69], off offset:-3072 nt
	global_load_dwordx4 v[56:59], v[68:69], off offset:-2048 nt
	global_load_dwordx4 v[60:63], v[68:69], off offset:-1024 nt
	global_load_dwordx4 v[64:67], v[68:69], off nt
	v_add_co_u32_e64 v28, s[0:1], s13, v26
	s_add_i32 s10, s10, s12
	s_nop 0
	v_addc_co_u32_e64 v29, s[0:1], -1, v27, s[0:1]
	s_cmp_lt_i32 s10, 0x10000
	v_lshl_add_u64 v[26:27], v[26:27], 0, s[14:15]
	s_waitcnt vmcnt(0)
	v_lshlrev_b32_e32 v30, 16, v22
	v_and_b32_e32 v22, 0xffff0000, v22
	v_lshlrev_b32_e32 v31, 16, v23
	v_and_b32_e32 v23, 0xffff0000, v23
	v_lshlrev_b32_e32 v68, 16, v24
	v_and_b32_e32 v24, 0xffff0000, v24
	v_lshlrev_b32_e32 v69, 16, v25
	v_and_b32_e32 v25, 0xffff0000, v25
	v_lshlrev_b32_e32 v70, 16, v18
	v_and_b32_e32 v18, 0xffff0000, v18
	v_lshlrev_b32_e32 v71, 16, v19
	v_and_b32_e32 v19, 0xffff0000, v19
	v_lshlrev_b32_e32 v72, 16, v20
	v_and_b32_e32 v20, 0xffff0000, v20
	v_lshlrev_b32_e32 v73, 16, v21
	v_and_b32_e32 v21, 0xffff0000, v21
	v_lshlrev_b32_e32 v74, 16, v14
	v_and_b32_e32 v14, 0xffff0000, v14
	v_lshlrev_b32_e32 v75, 16, v15
	v_and_b32_e32 v15, 0xffff0000, v15
	v_lshlrev_b32_e32 v76, 16, v16
	v_and_b32_e32 v16, 0xffff0000, v16
	v_lshlrev_b32_e32 v77, 16, v17
	v_and_b32_e32 v17, 0xffff0000, v17
	v_lshlrev_b32_e32 v78, 16, v10
	v_and_b32_e32 v10, 0xffff0000, v10
	v_lshlrev_b32_e32 v79, 16, v11
	v_and_b32_e32 v11, 0xffff0000, v11
	v_lshlrev_b32_e32 v80, 16, v12
	v_and_b32_e32 v12, 0xffff0000, v12
	v_lshlrev_b32_e32 v81, 16, v13
	v_and_b32_e32 v13, 0xffff0000, v13
	v_lshlrev_b32_e32 v94, 16, v36
	v_lshlrev_b32_e32 v108, 16, v52
	v_mul_f32_e32 v30, 0xbfb8aa3b, v30
	v_mul_f32_e32 v22, 0xbfb8aa3b, v22
	v_mul_f32_e32 v31, 0xbfb8aa3b, v31
	v_mul_f32_e32 v23, 0xbfb8aa3b, v23
	v_mul_f32_e32 v24, 0xbfb8aa3b, v24
	v_mul_f32_e32 v25, 0xbfb8aa3b, v25
	v_mul_f32_e32 v82, 0xbfb8aa3b, v18
	v_mul_f32_e32 v83, 0xbfb8aa3b, v19
	v_mul_f32_e32 v84, 0xbfb8aa3b, v20
	v_mul_f32_e32 v85, 0xbfb8aa3b, v21
	v_mul_f32_e32 v86, 0xbfb8aa3b, v14
	v_mul_f32_e32 v87, 0xbfb8aa3b, v15
	v_mul_f32_e32 v88, 0xbfb8aa3b, v16
	v_mul_f32_e32 v89, 0xbfb8aa3b, v17
	v_mul_f32_e32 v90, 0xbfb8aa3b, v10
	v_mul_f32_e32 v91, 0xbfb8aa3b, v11
	v_mul_f32_e32 v92, 0xbfb8aa3b, v12
	v_mul_f32_e32 v93, 0xbfb8aa3b, v13
	v_and_b32_e32 v95, 0xffff0000, v36
	v_lshlrev_b32_e32 v11, 16, v37
	v_and_b32_e32 v10, 0xffff0000, v37
	v_lshlrev_b32_e32 v13, 16, v38
	v_and_b32_e32 v12, 0xffff0000, v38
	v_lshlrev_b32_e32 v15, 16, v39
	v_and_b32_e32 v14, 0xffff0000, v39
	v_lshlrev_b32_e32 v102, 16, v40
	v_and_b32_e32 v103, 0xffff0000, v40
	v_lshlrev_b32_e32 v17, 16, v41
	v_and_b32_e32 v16, 0xffff0000, v41
	v_lshlrev_b32_e32 v19, 16, v42
	v_and_b32_e32 v18, 0xffff0000, v42
	v_lshlrev_b32_e32 v21, 16, v43
	v_and_b32_e32 v20, 0xffff0000, v43
	v_lshlrev_b32_e32 v104, 16, v44
	v_lshlrev_b32_e32 v106, 16, v48
	v_and_b32_e32 v107, 0xffff0000, v48
	v_lshlrev_b32_e32 v37, 16, v49
	v_and_b32_e32 v36, 0xffff0000, v49
	v_lshlrev_b32_e32 v39, 16, v50
	v_and_b32_e32 v38, 0xffff0000, v50
	v_lshlrev_b32_e32 v41, 16, v51
	v_and_b32_e32 v40, 0xffff0000, v51
	v_and_b32_e32 v109, 0xffff0000, v52
	v_lshlrev_b32_e32 v43, 16, v53
	v_and_b32_e32 v42, 0xffff0000, v53
	v_lshlrev_b32_e32 v110, 16, v56
	v_and_b32_e32 v111, 0xffff0000, v56
	v_lshlrev_b32_e32 v49, 16, v57
	v_and_b32_e32 v48, 0xffff0000, v57
	v_lshlrev_b32_e32 v51, 16, v58
	v_and_b32_e32 v50, 0xffff0000, v58
	v_lshlrev_b32_e32 v53, 16, v59
	v_and_b32_e32 v52, 0xffff0000, v59
	v_lshlrev_b32_e32 v112, 16, v60
	v_lshlrev_b32_e32 v57, 16, v62
	v_and_b32_e32 v56, 0xffff0000, v62
	v_lshlrev_b32_e32 v59, 16, v63
	v_and_b32_e32 v58, 0xffff0000, v63
	v_lshlrev_b32_e32 v114, 16, v64
; __device__ __forceinline__ float bflo(unsigned w) { return __uint_as_float(w << 16); }
; __device__ __forceinline__ float bfhi(unsigned w) { return __uint_as_float(w & 0xffff0000u); }
; __device__ __forceinline__ void p5_pool_yb(const Args& a, const Frame& F) {
;     ...
;             float v[8];
;             v[0] = bflo(f[u].x) + bflo(bk[u].x); v[1] = bfhi(f[u].x) + bfhi(bk[u].x); v[2] = bflo(f[u].y) + bflo(bk[u].y); v[3] = bfhi(f[u].y) + bfhi(bk[u].y);
;             v[4] = bflo(f[u].z) + bflo(bk[u].z); v[5] = bfhi(f[u].z) + bfhi(bk[u].z); v[6] = bflo(f[u].w) + bflo(bk[u].w); v[7] = bfhi(f[u].w) + bfhi(bk[u].w);
;             float s2 = 0.f;
; #pragma unroll
;             for (int jj = 0; jj < 8; ++jj) s2 += v[jj] * v[jj];
; #pragma unroll
;             for (int o = 1; o < 16; o <<= 1) s2 += __shfl_xor(s2, o);
;             const float rstd = rsqrtf(s2 * (1.f / 128.f) + EPS);
	v_lshlrev_b32_e32 v63, 16, v66
	v_and_b32_e32 v62, 0xffff0000, v66
	v_add_f32_e32 v66, v108, v94
	v_exp_f32_e32 v96, v30
	v_exp_f32_e32 v97, v22
	v_exp_f32_e32 v98, v31
	v_exp_f32_e32 v99, v23
	v_exp_f32_e32 v100, v24
	v_exp_f32_e32 v101, v25
	v_and_b32_e32 v105, 0xffff0000, v44
	v_lshlrev_b32_e32 v23, 16, v45
	v_and_b32_e32 v22, 0xffff0000, v45
	v_lshlrev_b32_e32 v25, 16, v46
	v_and_b32_e32 v24, 0xffff0000, v46
	v_lshlrev_b32_e32 v31, 16, v47
	v_and_b32_e32 v30, 0xffff0000, v47
	v_lshlrev_b32_e32 v45, 16, v54
	v_and_b32_e32 v44, 0xffff0000, v54
	v_lshlrev_b32_e32 v47, 16, v55
	v_and_b32_e32 v46, 0xffff0000, v55
	v_and_b32_e32 v113, 0xffff0000, v60
	v_lshlrev_b32_e32 v55, 16, v61
	v_and_b32_e32 v54, 0xffff0000, v61
	v_and_b32_e32 v115, 0xffff0000, v64
	v_lshlrev_b32_e32 v61, 16, v65
	v_and_b32_e32 v60, 0xffff0000, v65
	v_lshlrev_b32_e32 v65, 16, v67
	v_and_b32_e32 v64, 0xffff0000, v67
	v_add_f32_e32 v67, v109, v95
	v_pk_add_f32 v[10:11], v[10:11], v[42:43]
	v_add_f32_e32 v94, v110, v102
	v_add_f32_e32 v102, v112, v104
	v_add_f32_e32 v104, v114, v106
	v_mul_f32_e32 v106, v66, v66
	v_pk_mul_f32 v[42:43], v[10:11], v[10:11]
	v_fmac_f32_e32 v106, v67, v67
	v_pk_add_f32 v[12:13], v[12:13], v[44:45]
	v_add_f32_e32 v95, v111, v103
	v_pk_add_f32 v[16:17], v[16:17], v[48:49]
	v_add_f32_e32 v103, v113, v105
	v_pk_add_f32 v[22:23], v[22:23], v[54:55]
	v_add_f32_e32 v105, v115, v107
	v_pk_add_f32 v[36:37], v[36:37], v[60:61]
	v_mul_f32_e32 v107, v94, v94
	v_mul_f32_e32 v108, v102, v102
	v_mul_f32_e32 v109, v104, v104
	v_add_f32_e32 v43, v43, v106
	v_pk_mul_f32 v[44:45], v[12:13], v[12:13]
	v_pk_mul_f32 v[48:49], v[16:17], v[16:17]
	v_pk_mul_f32 v[54:55], v[22:23], v[22:23]
	v_pk_mul_f32 v[60:61], v[36:37], v[36:37]
	v_fmac_f32_e32 v107, v95, v95
	v_fmac_f32_e32 v108, v103, v103
	v_fmac_f32_e32 v109, v105, v105
	v_add_f32_e32 v42, v42, v43
	v_pk_add_f32 v[14:15], v[14:15], v[46:47]
	v_pk_add_f32 v[18:19], v[18:19], v[50:51]
	v_pk_add_f32 v[24:25], v[24:25], v[56:57]
	v_pk_add_f32 v[38:39], v[38:39], v[62:63]
	v_add_f32_e32 v49, v49, v107
	v_add_f32_e32 v55, v55, v108
	v_add_f32_e32 v61, v61, v109
	v_add_f32_e32 v42, v45, v42
	v_pk_mul_f32 v[46:47], v[14:15], v[14:15]
	v_pk_mul_f32 v[50:51], v[18:19], v[18:19]
	v_pk_mul_f32 v[56:57], v[24:25], v[24:25]
	v_pk_mul_f32 v[62:63], v[38:39], v[38:39]
	v_add_f32_e32 v43, v48, v49
	v_add_f32_e32 v48, v54, v55
	v_add_f32_e32 v49, v60, v61
	v_add_f32_e32 v42, v44, v42
	v_pk_add_f32 v[20:21], v[20:21], v[52:53]
	v_pk_add_f32 v[30:31], v[30:31], v[58:59]
	v_pk_add_f32 v[40:41], v[40:41], v[64:65]
	v_add_f32_e32 v43, v51, v43
	v_add_f32_e32 v45, v57, v48
	v_add_f32_e32 v48, v63, v49
	v_add_f32_e32 v42, v47, v42
	v_pk_mul_f32 v[52:53], v[20:21], v[20:21]
	v_pk_mul_f32 v[58:59], v[30:31], v[30:31]
	v_pk_mul_f32 v[64:65], v[40:41], v[40:41]
	v_add_f32_e32 v43, v50, v43
	v_add_f32_e32 v44, v56, v45
	v_add_f32_e32 v45, v62, v48
	v_add_f32_e32 v42, v46, v42
	v_add_f32_e32 v43, v53, v43
	v_add_f32_e32 v44, v59, v44
	v_add_f32_e32 v45, v65, v45
	ds_bpermute_b32 v46, v1, v42
	v_add_f32_e32 v43, v52, v43
	v_add_f32_e32 v44, v58, v44
	v_add_f32_e32 v45, v64, v45
	ds_bpermute_b32 v47, v1, v43
	ds_bpermute_b32 v48, v1, v44
	ds_bpermute_b32 v49, v1, v45
	s_waitcnt lgkmcnt(3)
	v_add_f32_e32 v42, v42, v46
	ds_bpermute_b32 v46, v32, v42
	s_waitcnt lgkmcnt(3)
	v_add_f32_e32 v43, v43, v47
	s_waitcnt lgkmcnt(2)
	v_add_f32_e32 v44, v44, v48
	s_waitcnt lgkmcnt(1)
	v_add_f32_e32 v45, v45, v49
	ds_bpermute_b32 v47, v32, v43
	ds_bpermute_b32 v48, v32, v44
	ds_bpermute_b32 v49, v32, v45
	s_waitcnt lgkmcnt(3)
	v_add_f32_e32 v42, v42, v46
	ds_bpermute_b32 v46, v33, v42
	s_waitcnt lgkmcnt(3)
	v_add_f32_e32 v43, v43, v47
	s_waitcnt lgkmcnt(2)
	v_add_f32_e32 v44, v44, v48
	s_waitcnt lgkmcnt(1)
	v_add_f32_e32 v45, v45, v49
	ds_bpermute_b32 v47, v33, v43
	ds_bpermute_b32 v48, v33, v44
	ds_bpermute_b32 v49, v33, v45
	s_waitcnt lgkmcnt(3)
	v_add_f32_e32 v42, v42, v46
	ds_bpermute_b32 v46, v34, v42
	s_waitcnt lgkmcnt(3)
	v_add_f32_e32 v43, v43, v47
	s_waitcnt lgkmcnt(2)
	v_add_f32_e32 v44, v44, v48
	s_waitcnt lgkmcnt(1)
	v_add_f32_e32 v45, v45, v49
	ds_bpermute_b32 v47, v34, v43
	ds_bpermute_b32 v48, v34, v44
	ds_bpermute_b32 v49, v34, v45
	s_waitcnt lgkmcnt(3)
	v_add_f32_e32 v42, v42, v46
	v_fmamk_f32 v42, v42, 0x3c000000, v35
	v_mul_f32_e32 v68, 0xbfb8aa3b, v68
	s_waitcnt lgkmcnt(2)
	v_add_f32_e32 v43, v43, v47
	s_waitcnt lgkmcnt(1)
	v_add_f32_e32 v44, v44, v48
	s_waitcnt lgkmcnt(0)
; __device__ __forceinline__ float bflo(unsigned w) { return __uint_as_float(w << 16); }
; __device__ __forceinline__ float bfhi(unsigned w) { return __uint_as_float(w & 0xffff0000u); }
; __device__ __forceinline__ float sigmoidf_(float x) { return frcp_(1.0f + fexp_(-x)); }
; __device__ __forceinline__ void p5_pool_yb(const Args& a, const Frame& F) {
;     ...
;             const float rstd = rsqrtf(s2 * (1.f / 128.f) + EPS);
;             float gsig[8];
;             gsig[0] = sigmoidf_(bflo(og[u].x)); gsig[1] = sigmoidf_(bfhi(og[u].x)); gsig[2] = sigmoidf_(bflo(og[u].y)); gsig[3] = sigmoidf_(bfhi(og[u].y));
;             gsig[4] = sigmoidf_(bflo(og[u].z)); gsig[5] = sigmoidf_(bfhi(og[u].z)); gsig[6] = sigmoidf_(bflo(og[u].w)); gsig[7] = sigmoidf_(bfhi(og[u].w));
;             float r[8];
; #pragma unroll
;             for (int jj = 0; jj < 8; ++jj) r[jj] = v[jj] * rstd * hwv[jj] * gsig[jj];
	v_add_f32_e32 v45, v45, v49
	v_mul_f32_e32 v46, 0x4b800000, v42
	v_cmp_gt_f32_e64 s[6:7], s11, v42
	v_mul_f32_e32 v69, 0xbfb8aa3b, v69
	v_exp_f32_e32 v68, v68
	v_fmamk_f32 v43, v43, 0x3c000000, v35
	v_fmamk_f32 v44, v44, 0x3c000000, v35
	v_fmamk_f32 v45, v45, 0x3c000000, v35
	v_cndmask_b32_e64 v42, v42, v46, s[6:7]
	v_mul_f32_e32 v70, 0xbfb8aa3b, v70
	v_mul_f32_e32 v71, 0xbfb8aa3b, v71
	v_mul_f32_e32 v72, 0xbfb8aa3b, v72
	v_mul_f32_e32 v73, 0xbfb8aa3b, v73
	v_exp_f32_e32 v69, v69
	v_mul_f32_e32 v47, 0x4b800000, v43
	v_cmp_gt_f32_e32 vcc, s11, v43
	v_mul_f32_e32 v48, 0x4b800000, v44
	v_cmp_gt_f32_e64 s[0:1], s11, v44
	v_mul_f32_e32 v49, 0x4b800000, v45
	v_cmp_gt_f32_e64 s[4:5], s11, v45
	v_rsq_f32_e32 v42, v42
	v_mul_f32_e32 v74, 0xbfb8aa3b, v74
	v_mul_f32_e32 v75, 0xbfb8aa3b, v75
	v_mul_f32_e32 v76, 0xbfb8aa3b, v76
	v_mul_f32_e32 v77, 0xbfb8aa3b, v77
	v_exp_f32_e32 v70, v70
	v_exp_f32_e32 v82, v82
	v_exp_f32_e32 v71, v71
	v_exp_f32_e32 v83, v83
	v_exp_f32_e32 v72, v72
	v_exp_f32_e32 v84, v84
	v_exp_f32_e32 v73, v73
	v_exp_f32_e32 v85, v85
	v_cndmask_b32_e32 v43, v43, v47, vcc
	v_cndmask_b32_e64 v44, v44, v48, s[0:1]
	v_cndmask_b32_e64 v45, v45, v49, s[4:5]
	v_mul_f32_e32 v78, 0xbfb8aa3b, v78
	v_mul_f32_e32 v79, 0xbfb8aa3b, v79
	v_mul_f32_e32 v80, 0xbfb8aa3b, v80
	v_mul_f32_e32 v81, 0xbfb8aa3b, v81
	v_exp_f32_e32 v74, v74
	v_exp_f32_e32 v86, v86
	v_exp_f32_e32 v75, v75
	v_exp_f32_e32 v87, v87
	v_exp_f32_e32 v76, v76
	v_exp_f32_e32 v88, v88
	v_exp_f32_e32 v77, v77
	v_exp_f32_e32 v89, v89
	v_rsq_f32_e32 v43, v43
	v_rsq_f32_e32 v44, v44
	v_rsq_f32_e32 v45, v45
	v_exp_f32_e32 v78, v78
	v_exp_f32_e32 v90, v90
	v_exp_f32_e32 v79, v79
	v_exp_f32_e32 v91, v91
	v_exp_f32_e32 v80, v80
	v_exp_f32_e32 v92, v92
	v_exp_f32_e32 v81, v81
	v_exp_f32_e32 v93, v93
	v_add_f32_e32 v98, 1.0, v98
	v_add_f32_e32 v68, 1.0, v68
	v_add_f32_e32 v100, 1.0, v100
	v_add_f32_e32 v96, 1.0, v96
	v_add_f32_e32 v97, 1.0, v97
	v_add_f32_e32 v99, 1.0, v99
	v_add_f32_e32 v69, 1.0, v69
	v_add_f32_e32 v101, 1.0, v101
	v_rcp_f32_e32 v98, v98
	v_rcp_f32_e32 v68, v68
	v_rcp_f32_e32 v100, v100
	v_mul_f32_e32 v46, 0x45800000, v42
	v_add_f32_e32 v70, 1.0, v70
	v_add_f32_e32 v82, 1.0, v82
	v_add_f32_e32 v71, 1.0, v71
	v_add_f32_e32 v83, 1.0, v83
	v_add_f32_e32 v72, 1.0, v72
	v_add_f32_e32 v84, 1.0, v84
	v_add_f32_e32 v73, 1.0, v73
	v_add_f32_e32 v85, 1.0, v85
	v_rcp_f32_e32 v96, v96
	v_rcp_f32_e32 v97, v97
	v_rcp_f32_e32 v99, v99
	v_rcp_f32_e32 v69, v69
	v_rcp_f32_e32 v101, v101
	v_cndmask_b32_e64 v42, v42, v46, s[6:7]
	v_add_f32_e32 v74, 1.0, v74
	v_add_f32_e32 v86, 1.0, v86
	v_add_f32_e32 v75, 1.0, v75
	v_add_f32_e32 v87, 1.0, v87
	v_add_f32_e32 v76, 1.0, v76
	v_add_f32_e32 v88, 1.0, v88
	v_add_f32_e32 v77, 1.0, v77
	v_add_f32_e32 v89, 1.0, v89
	v_rcp_f32_e32 v70, v70
	v_rcp_f32_e32 v82, v82
	v_rcp_f32_e32 v71, v71
	v_rcp_f32_e32 v83, v83
	v_rcp_f32_e32 v72, v72
	v_rcp_f32_e32 v84, v84
	v_rcp_f32_e32 v73, v73
	v_rcp_f32_e32 v85, v85
	v_mul_f32_e32 v47, 0x45800000, v43
	v_mul_f32_e32 v48, 0x45800000, v44
	v_mul_f32_e32 v49, 0x45800000, v45
	v_mul_f32_e32 v11, v11, v42
	v_mul_f32_e32 v13, v13, v42
	v_mul_f32_e32 v12, v12, v42
	v_add_f32_e32 v78, 1.0, v78
	v_add_f32_e32 v90, 1.0, v90
	v_add_f32_e32 v79, 1.0, v79
	v_add_f32_e32 v91, 1.0, v91
	v_add_f32_e32 v80, 1.0, v80
	v_add_f32_e32 v92, 1.0, v92
	v_add_f32_e32 v81, 1.0, v81
	v_add_f32_e32 v93, 1.0, v93
	v_rcp_f32_e32 v74, v74
	v_rcp_f32_e32 v86, v86
	v_rcp_f32_e32 v75, v75
	v_rcp_f32_e32 v87, v87
	v_rcp_f32_e32 v76, v76
	v_rcp_f32_e32 v88, v88
	v_rcp_f32_e32 v77, v77
	v_rcp_f32_e32 v89, v89
	v_cndmask_b32_e32 v43, v43, v47, vcc
	v_cndmask_b32_e64 v44, v44, v48, s[0:1]
	v_cndmask_b32_e64 v45, v45, v49, s[4:5]
; __device__ __forceinline__ unsigned cvt_pk_bf16(float lo, float hi) { unsigned r; asm volatile("v_cvt_pk_bf16_f32 %0, %1, %2" : "=v"(r) : "v"(lo), "v"(hi)); return r; }
; __device__ __forceinline__ void p5_pool_yb(const Args& a, const Frame& F) {
;     ...
;             float r[8];
; #pragma unroll
;             for (int jj = 0; jj < 8; ++jj) r[jj] = v[jj] * rstd * hwv[jj] * gsig[jj];
;             u32x4 wv; wv.x = pg8::cvt_pk_bf16(r[0], r[1]); wv.y = pg8::cvt_pk_bf16(r[2], r[3]); wv.z = pg8::cvt_pk_bf16(r[4], r[5]); wv.w = pg8::cvt_pk_bf16(r[6], r[7]);
;             *(u32x4*)(YB + (size_t)(t0 + u) * 512 + F.lane * 8) = wv;
;         }
	v_mul_f32_e32 v46, v66, v42
	v_mul_f32_e32 v47, v67, v42
	v_mul_f32_e32 v10, v10, v42
	v_mul_f32_e32 v15, v15, v42
	v_mul_f32_e32 v14, v14, v42
	v_mul_f32_e32 v11, v4, v11
	v_mul_f32_e32 v13, v6, v13
	v_mul_f32_e32 v12, v7, v12
	v_rcp_f32_e32 v78, v78
	v_rcp_f32_e32 v90, v90
	v_rcp_f32_e32 v79, v79
	v_rcp_f32_e32 v91, v91
	v_rcp_f32_e32 v80, v80
	v_rcp_f32_e32 v92, v92
	v_rcp_f32_e32 v81, v81
	v_rcp_f32_e32 v93, v93
	v_mul_f32_e32 v42, v94, v43
	v_mul_f32_e32 v48, v95, v43
	v_mul_f32_e32 v17, v17, v43
	v_mul_f32_e32 v16, v16, v43
	v_mul_f32_e32 v19, v19, v43
	v_mul_f32_e32 v18, v18, v43
	v_mul_f32_e32 v21, v21, v43
	v_mul_f32_e32 v20, v20, v43
	v_mul_f32_e32 v43, v102, v44
	v_mul_f32_e32 v49, v103, v44
	v_mul_f32_e32 v23, v23, v44
	v_mul_f32_e32 v22, v22, v44
	v_mul_f32_e32 v25, v25, v44
	v_mul_f32_e32 v24, v24, v44
	v_mul_f32_e32 v31, v31, v44
	v_mul_f32_e32 v30, v30, v44
	v_mul_f32_e32 v44, v104, v45
	v_mul_f32_e32 v50, v105, v45
	v_mul_f32_e32 v37, v37, v45
	v_mul_f32_e32 v36, v36, v45
	v_mul_f32_e32 v39, v39, v45
	v_mul_f32_e32 v38, v38, v45
	v_mul_f32_e32 v41, v41, v45
	v_mul_f32_e32 v40, v40, v45
	v_mul_f32_e32 v45, v2, v46
	v_mul_f32_e32 v46, v3, v47
	v_mul_f32_e32 v10, v5, v10
	v_mul_f32_e32 v15, v8, v15
	v_mul_f32_e32 v14, v9, v14
	v_mul_f32_e32 v11, v98, v11
	v_mul_f32_e32 v13, v68, v13
	v_mul_f32_e32 v12, v100, v12
	v_mul_f32_e32 v42, v2, v42
	v_mul_f32_e32 v47, v3, v48
	v_mul_f32_e32 v17, v4, v17
	v_mul_f32_e32 v16, v5, v16
	v_mul_f32_e32 v19, v6, v19
	v_mul_f32_e32 v18, v7, v18
	v_mul_f32_e32 v21, v8, v21
	v_mul_f32_e32 v20, v9, v20
	v_mul_f32_e32 v48, v3, v49
	v_mul_f32_e32 v49, v3, v50
	v_mul_f32_e32 v45, v96, v45
	v_mul_f32_e32 v46, v97, v46
	v_mul_f32_e32 v50, v99, v10
	v_mul_f32_e32 v15, v69, v15
	v_mul_f32_e32 v14, v101, v14
	v_cvt_pk_bf16_f32 v10, v45, v46
	v_cvt_pk_bf16_f32 v11, v11, v50
	v_cvt_pk_bf16_f32 v12, v13, v12
	v_cvt_pk_bf16_f32 v13, v15, v14
	v_mul_f32_e32 v43, v2, v43
	v_mul_f32_e32 v23, v4, v23
	v_mul_f32_e32 v22, v5, v22
	v_mul_f32_e32 v25, v6, v25
	v_mul_f32_e32 v24, v7, v24
	v_mul_f32_e32 v31, v8, v31
	v_mul_f32_e32 v30, v9, v30
	v_mul_f32_e32 v42, v70, v42
	v_mul_f32_e32 v47, v82, v47
	v_mul_f32_e32 v17, v71, v17
	v_mul_f32_e32 v16, v83, v16
	v_mul_f32_e32 v19, v72, v19
	v_mul_f32_e32 v18, v84, v18
	v_mul_f32_e32 v21, v73, v21
	v_mul_f32_e32 v20, v85, v20
	global_store_dwordx4 v[28:29], v[10:13], off offset:-3072
	v_mul_f32_e32 v44, v2, v44
	v_mul_f32_e32 v37, v4, v37
	v_cvt_pk_bf16_f32 v10, v42, v47
	v_cvt_pk_bf16_f32 v11, v17, v16
	v_cvt_pk_bf16_f32 v12, v19, v18
	v_cvt_pk_bf16_f32 v13, v21, v20
	v_mul_f32_e32 v36, v5, v36
	v_mul_f32_e32 v39, v6, v39
	v_mul_f32_e32 v38, v7, v38
	v_mul_f32_e32 v41, v8, v41
	v_mul_f32_e32 v40, v9, v40
	v_mul_f32_e32 v43, v74, v43
	v_mul_f32_e32 v48, v86, v48
	v_mul_f32_e32 v23, v75, v23
	v_mul_f32_e32 v22, v87, v22
	v_mul_f32_e32 v25, v76, v25
	v_mul_f32_e32 v24, v88, v24
	v_mul_f32_e32 v31, v77, v31
	v_mul_f32_e32 v30, v89, v30
	global_store_dwordx4 v[28:29], v[10:13], off offset:-2048
	v_mul_f32_e32 v44, v78, v44
	v_mul_f32_e32 v49, v90, v49
	v_cvt_pk_bf16_f32 v10, v43, v48
	v_cvt_pk_bf16_f32 v11, v23, v22
	v_cvt_pk_bf16_f32 v12, v25, v24
	v_cvt_pk_bf16_f32 v13, v31, v30
	v_mul_f32_e32 v37, v79, v37
	v_mul_f32_e32 v36, v91, v36
	v_mul_f32_e32 v39, v80, v39
	v_mul_f32_e32 v38, v92, v38
	v_mul_f32_e32 v41, v81, v41
	v_mul_f32_e32 v40, v93, v40
	global_store_dwordx4 v[28:29], v[10:13], off offset:-1024
	s_nop 1
	v_cvt_pk_bf16_f32 v10, v44, v49
	v_cvt_pk_bf16_f32 v11, v37, v36
	v_cvt_pk_bf16_f32 v12, v39, v38
	v_cvt_pk_bf16_f32 v13, v41, v40
	global_store_dwordx4 v[28:29], v[10:13], off
	s_cbranch_scc1 .LBB0_579
